# v52 + redundant lgkmcnt waits removed from the P2/P6 MFMA bursts (the read segment already drains LDS before the barrier)
# baseline (speedup 1.0000x reference)
.LBB0_210:
	s_barrier
	v_mfma_f32_16x16x32_bf16 v[122:125], v[130:133], v[174:177], v[122:125]
	v_mfma_f32_16x16x32_bf16 v[126:129], v[134:137], v[174:177], v[126:129]
	v_mfma_f32_16x16x32_bf16 v[114:117], v[138:141], v[174:177], v[114:117]
	v_mfma_f32_16x16x32_bf16 v[110:113], v[142:145], v[174:177], v[110:113]
	v_mfma_f32_16x16x32_bf16 v[106:109], v[130:133], v[170:173], v[106:109]
	v_mfma_f32_16x16x32_bf16 v[118:121], v[134:137], v[170:173], v[118:121]
	v_mfma_f32_16x16x32_bf16 v[98:101], v[138:141], v[170:173], v[98:101]
	v_mfma_f32_16x16x32_bf16 v[94:97], v[142:145], v[170:173], v[94:97]
	v_mfma_f32_16x16x32_bf16 v[90:93], v[130:133], v[166:169], v[90:93]
	v_mfma_f32_16x16x32_bf16 v[102:105], v[134:137], v[166:169], v[102:105]
	v_mfma_f32_16x16x32_bf16 v[82:85], v[138:141], v[166:169], v[82:85]
	v_mfma_f32_16x16x32_bf16 v[78:81], v[142:145], v[166:169], v[78:81]
	v_mfma_f32_16x16x32_bf16 v[74:77], v[130:133], v[162:165], v[74:77]
	v_mfma_f32_16x16x32_bf16 v[86:89], v[134:137], v[162:165], v[86:89]
	v_mfma_f32_16x16x32_bf16 v[70:73], v[138:141], v[162:165], v[70:73]
	v_mfma_f32_16x16x32_bf16 v[62:65], v[142:145], v[162:165], v[62:65]
	v_mfma_f32_16x16x32_bf16 v[58:61], v[130:133], v[158:161], v[58:61]
	v_mfma_f32_16x16x32_bf16 v[66:69], v[134:137], v[158:161], v[66:69]
	v_mfma_f32_16x16x32_bf16 v[54:57], v[138:141], v[158:161], v[54:57]
	v_mfma_f32_16x16x32_bf16 v[46:49], v[142:145], v[158:161], v[46:49]
	v_mfma_f32_16x16x32_bf16 v[42:45], v[130:133], v[154:157], v[42:45]
	v_mfma_f32_16x16x32_bf16 v[50:53], v[134:137], v[154:157], v[50:53]
	v_mfma_f32_16x16x32_bf16 v[38:41], v[138:141], v[154:157], v[38:41]
	v_mfma_f32_16x16x32_bf16 v[34:37], v[142:145], v[154:157], v[34:37]
	v_mfma_f32_16x16x32_bf16 v[26:29], v[130:133], v[150:153], v[26:29]
	v_mfma_f32_16x16x32_bf16 v[30:33], v[134:137], v[150:153], v[30:33]
	v_mfma_f32_16x16x32_bf16 v[22:25], v[138:141], v[150:153], v[22:25]
	v_mfma_f32_16x16x32_bf16 v[18:21], v[142:145], v[150:153], v[18:21]
	v_mfma_f32_16x16x32_bf16 v[10:13], v[130:133], v[146:149], v[10:13]
	v_mfma_f32_16x16x32_bf16 v[14:17], v[134:137], v[146:149], v[14:17]
	v_mfma_f32_16x16x32_bf16 v[6:9], v[138:141], v[146:149], v[6:9]
	v_mfma_f32_16x16x32_bf16 v[2:5], v[142:145], v[146:149], v[2:5]
	s_add_i32 s85, s85, 1
	s_cmp_gt_u32 s85, 61
	s_cselect_b64 vcc, exec, 0
	s_cmp_eq_u32 s85, 64
	s_barrier
	s_cbranch_scc1 .Lp2_exit

.LBB0_614:
	s_barrier
	v_mfma_f32_16x16x32_bf16 v[126:129], v[130:133], v[174:177], v[126:129]
	v_mfma_f32_16x16x32_bf16 v[102:105], v[134:137], v[174:177], v[102:105]
	v_mfma_f32_16x16x32_bf16 v[70:73], v[138:141], v[174:177], v[70:73]
	v_mfma_f32_16x16x32_bf16 v[38:41], v[142:145], v[174:177], v[38:41]
	v_mfma_f32_16x16x32_bf16 v[122:125], v[130:133], v[170:173], v[122:125]
	v_mfma_f32_16x16x32_bf16 v[94:97], v[134:137], v[170:173], v[94:97]
	v_mfma_f32_16x16x32_bf16 v[62:65], v[138:141], v[170:173], v[62:65]
	v_mfma_f32_16x16x32_bf16 v[30:33], v[142:145], v[170:173], v[30:33]
	v_mfma_f32_16x16x32_bf16 v[118:121], v[130:133], v[166:169], v[118:121]
	v_mfma_f32_16x16x32_bf16 v[86:89], v[134:137], v[166:169], v[86:89]
	v_mfma_f32_16x16x32_bf16 v[54:57], v[138:141], v[166:169], v[54:57]
	v_mfma_f32_16x16x32_bf16 v[22:25], v[142:145], v[166:169], v[22:25]
	v_mfma_f32_16x16x32_bf16 v[114:117], v[130:133], v[162:165], v[114:117]
	v_mfma_f32_16x16x32_bf16 v[82:85], v[134:137], v[162:165], v[82:85]
	v_mfma_f32_16x16x32_bf16 v[50:53], v[138:141], v[162:165], v[50:53]
	v_mfma_f32_16x16x32_bf16 v[18:21], v[142:145], v[162:165], v[18:21]
	v_mfma_f32_16x16x32_bf16 v[110:113], v[130:133], v[158:161], v[110:113]
	v_mfma_f32_16x16x32_bf16 v[78:81], v[134:137], v[158:161], v[78:81]
	v_mfma_f32_16x16x32_bf16 v[46:49], v[138:141], v[158:161], v[46:49]
	v_mfma_f32_16x16x32_bf16 v[14:17], v[142:145], v[158:161], v[14:17]
	v_mfma_f32_16x16x32_bf16 v[106:109], v[130:133], v[154:157], v[106:109]
	v_mfma_f32_16x16x32_bf16 v[74:77], v[134:137], v[154:157], v[74:77]
	v_mfma_f32_16x16x32_bf16 v[42:45], v[138:141], v[154:157], v[42:45]
	v_mfma_f32_16x16x32_bf16 v[10:13], v[142:145], v[154:157], v[10:13]
	v_mfma_f32_16x16x32_bf16 v[98:101], v[130:133], v[150:153], v[98:101]
	v_mfma_f32_16x16x32_bf16 v[66:69], v[134:137], v[150:153], v[66:69]
	v_mfma_f32_16x16x32_bf16 v[34:37], v[138:141], v[150:153], v[34:37]
	v_mfma_f32_16x16x32_bf16 v[6:9], v[142:145], v[150:153], v[6:9]
	v_mfma_f32_16x16x32_bf16 v[90:93], v[130:133], v[146:149], v[90:93]
	v_mfma_f32_16x16x32_bf16 v[58:61], v[134:137], v[146:149], v[58:61]
	v_mfma_f32_16x16x32_bf16 v[26:29], v[138:141], v[146:149], v[26:29]
	v_mfma_f32_16x16x32_bf16 v[2:5], v[142:145], v[146:149], v[2:5]
	s_add_i32 s61, s61, 1
	s_cmp_gt_u32 s61, 61
	s_cselect_b64 vcc, exec, 0
	s_cmp_eq_u32 s61, 64
	s_barrier
	s_cbranch_scc1 .Lp6_exit
